# static priority for waves 0-3 + their unit-end alignment barrier moved behind the 2nd SwiGLU row group (prioritised half starts its epilogue during the other half's last MFMA block)
# baseline (speedup 1.0000x reference)
; #define PG8_STAGE(bufoff, gbase, voff) do { _Pragma("unroll") for (int _i = 0; _i < 2; ++_i) \
;         __builtin_amdgcn_global_load_lds((const unsigned*)((const char*)(gbase) + (voff)[_i]), (PG8_LAS unsigned*)(lds + (bufoff) + ldsw + _i * 8192), 16, 0, 0); } while (0)
; #define PG8_LDA(dst, b, h) do { _Pragma("unroll") for (int m = 0; m < 4; ++m) _Pragma("unroll") for (int k = 0; k < 2; ++k) dst[m][k] = *(const PG8_LAS bf16x8*)(lds + PG8_SA(b, h) + aoff + m * 2048 + k * 1024); } while (0)
; #define PG8_LDB(dst, b, h) do { _Pragma("unroll") for (int n = 0; n < 2; ++n) _Pragma("unroll") for (int k = 0; k < 2; ++k) dst[n][k] = *(const PG8_LAS bf16x8*)(lds + PG8_SB(b, h) + boff + n * 2048 + k * 1024); } while (0)
; #define PG8_MMA(ai, bj, At, Bt) do { __builtin_amdgcn_s_setprio(1); _Pragma("unroll") for (int m = 0; m < 4; ++m) _Pragma("unroll") for (int n = 0; n < 2; ++n) _Pragma("unroll") for (int k = 0; k < 2; ++k) \
;         acc[ai][bj][m][n] = __builtin_amdgcn_mfma_f32_16x16x32_bf16(Bt[n][k], At[m][k], acc[ai][bj][m][n], 0, 0, 0); __builtin_amdgcn_s_setprio(0); } while (0)
; #define PG8_WAIT_V(n) asm volatile("s_waitcnt vmcnt(" #n ")" ::: "memory")
; #define PG8_WAIT_L(n) asm volatile("s_waitcnt lgkmcnt(" #n ")" ::: "memory")
; #define PG8_BAR __builtin_amdgcn_s_barrier()
; #define PG8_SCHED __builtin_amdgcn_sched_barrier(0)
; template <class Epi, class Sched, bool ALIGN_EPI>
; __device__ __forceinline__ void gemm_phase(PG8_LAS unsigned char* lds, const Gemm g, const Sched& S, const Epi& E, const int tid) {
;     ...
;             PG8_LDB(B0, 0, 0); PG8_LDB(B1, 0, 1); PG8_SCHED; PG8_LDA(At, 0, 0); PG8_STAGE(PG8_SA(1, 1), a1 + hstepA, voffA);
;             PG8_WAIT_V(8); PG8_WAIT_L(0); PG8_BAR; PG8_MMA(0, 0, At, B0); PG8_MMA(0, 1, At, B1); PG8_BAR; PG8_SCHED;
;             PG8_LDA(At, 0, 1); PG8_STAGE(PG8_SB(0, 0), b2, voffB); PG8_STAGE(PG8_SB(0, 1), b2 + hstepB, voffB); PG8_STAGE(PG8_SA(0, 0), a2, voffA);
;             PG8_WAIT_V(8); PG8_WAIT_L(0); PG8_BAR; PG8_MMA(1, 0, At, B0); PG8_MMA(1, 1, At, B1); PG8_BAR; PG8_SCHED;
;             PG8_LDB(B0, 1, 0); PG8_LDB(B1, 1, 1); PG8_SCHED; PG8_LDA(At, 1, 0); PG8_STAGE(PG8_SA(0, 1), a2 + hstepA, voffA);
;             PG8_WAIT_V(8); PG8_WAIT_L(0); PG8_BAR; PG8_MMA(0, 0, At, B0); PG8_MMA(0, 1, At, B1); PG8_BAR; PG8_SCHED;
.Lsprio_0:
	s_barrier
	v_mfma_f32_16x16x32_bf16 v[142:145], v[80:83], v[194:197], 0
	v_mfma_f32_16x16x32_bf16 v[134:137], v[96:99], v[194:197], 0
	v_mfma_f32_16x16x32_bf16 v[124:127], v[80:83], v[202:205], 0
	v_mfma_f32_16x16x32_bf16 v[116:119], v[96:99], v[202:205], 0
	v_mfma_f32_16x16x32_bf16 v[108:111], v[80:83], v[210:213], 0
	v_mfma_f32_16x16x32_bf16 v[92:95], v[96:99], v[210:213], 0
	v_mfma_f32_16x16x32_bf16 v[76:79], v[80:83], v[218:221], 0
	v_mfma_f32_16x16x32_bf16 v[68:71], v[96:99], v[218:221], 0
	v_mfma_f32_16x16x32_bf16 v[142:145], v[84:87], v[198:201], v[142:145]
	v_mfma_f32_16x16x32_bf16 v[134:137], v[100:103], v[198:201], v[134:137]
	v_mfma_f32_16x16x32_bf16 v[124:127], v[84:87], v[206:209], v[124:127]
	v_mfma_f32_16x16x32_bf16 v[116:119], v[100:103], v[206:209], v[116:119]
	v_mfma_f32_16x16x32_bf16 v[108:111], v[84:87], v[214:217], v[108:111]
	v_mfma_f32_16x16x32_bf16 v[92:95], v[100:103], v[214:217], v[92:95]
	v_mfma_f32_16x16x32_bf16 v[76:79], v[84:87], v[222:225], v[76:79]
	v_mfma_f32_16x16x32_bf16 v[68:71], v[100:103], v[222:225], v[68:71]
	v_mfma_f32_16x16x32_bf16 v[138:141], v[162:165], v[194:197], 0
	v_mfma_f32_16x16x32_bf16 v[130:133], v[186:189], v[194:197], 0
	v_mfma_f32_16x16x32_bf16 v[120:123], v[162:165], v[202:205], 0
	v_mfma_f32_16x16x32_bf16 v[112:115], v[186:189], v[202:205], 0
	v_mfma_f32_16x16x32_bf16 v[104:107], v[162:165], v[210:213], 0
	v_mfma_f32_16x16x32_bf16 v[88:91], v[186:189], v[210:213], 0
	v_mfma_f32_16x16x32_bf16 v[72:75], v[162:165], v[218:221], 0
	v_mfma_f32_16x16x32_bf16 v[64:67], v[186:189], v[218:221], 0
	v_mfma_f32_16x16x32_bf16 v[138:141], v[182:185], v[198:201], v[138:141]
	v_mfma_f32_16x16x32_bf16 v[130:133], v[190:193], v[198:201], v[130:133]
	v_mfma_f32_16x16x32_bf16 v[120:123], v[182:185], v[206:209], v[120:123]
	v_mfma_f32_16x16x32_bf16 v[112:115], v[190:193], v[206:209], v[112:115]
	v_mfma_f32_16x16x32_bf16 v[104:107], v[182:185], v[214:217], v[104:107]
	v_mfma_f32_16x16x32_bf16 v[88:91], v[190:193], v[214:217], v[88:91]
	v_mfma_f32_16x16x32_bf16 v[72:75], v[182:185], v[222:225], v[72:75]
	v_mfma_f32_16x16x32_bf16 v[64:67], v[190:193], v[222:225], v[64:67]
	s_barrier
	s_add_i32 s63, s63, s42
	s_mov_b32 m0, s63
	ds_read_b128 v[194:197], v180 offset:16384
	ds_read_b128 v[198:201], v180 offset:17408
	ds_read_b128 v[202:205], v180 offset:18432
	ds_read_b128 v[206:209], v180 offset:19456
	ds_read_b128 v[210:213], v180 offset:20480
	ds_read_b128 v[214:217], v180 offset:21504
	ds_read_b128 v[218:221], v180 offset:22528
	ds_read_b128 v[222:225], v180 offset:23552
	global_load_lds_dwordx4 v150, s[20:21]
	s_add_i32 m0, s63, 0x2000
	s_add_u32 s64, s20, 0x4000
	s_addc_u32 s65, s21, 0
	s_add_i32 s63, s66, s42
	global_load_lds_dwordx4 v146, s[20:21]
	s_mov_b32 m0, s63
	s_nop 0
	global_load_lds_dwordx4 v150, s[64:65]
	s_add_i32 m0, s63, 0x2000
	s_nop 0
	global_load_lds_dwordx4 v146, s[64:65]
	s_mov_b32 m0, s45
	s_nop 0
	global_load_lds_dwordx4 v152, s[22:23]
	s_mov_b32 m0, s46
	s_nop 0
	global_load_lds_dwordx4 v148, s[22:23]
	s_waitcnt vmcnt(8)
	s_waitcnt lgkmcnt(0)
	s_barrier
	v_mfma_f32_16x16x32_bf16 v[60:63], v[80:83], v[194:197], 0
	v_mfma_f32_16x16x32_bf16 v[52:55], v[96:99], v[194:197], 0
	v_mfma_f32_16x16x32_bf16 v[44:47], v[80:83], v[202:205], 0
	v_mfma_f32_16x16x32_bf16 v[36:39], v[96:99], v[202:205], 0
	v_mfma_f32_16x16x32_bf16 v[28:31], v[80:83], v[210:213], 0
	v_mfma_f32_16x16x32_bf16 v[20:23], v[96:99], v[210:213], 0
	v_mfma_f32_16x16x32_bf16 v[12:15], v[80:83], v[218:221], 0
	v_mfma_f32_16x16x32_bf16 v[4:7], v[96:99], v[218:221], 0
	v_mfma_f32_16x16x32_bf16 v[60:63], v[84:87], v[198:201], v[60:63]
	v_mfma_f32_16x16x32_bf16 v[52:55], v[100:103], v[198:201], v[52:55]
	v_mfma_f32_16x16x32_bf16 v[44:47], v[84:87], v[206:209], v[44:47]
	v_mfma_f32_16x16x32_bf16 v[36:39], v[100:103], v[206:209], v[36:39]
	v_mfma_f32_16x16x32_bf16 v[28:31], v[84:87], v[214:217], v[28:31]
	v_mfma_f32_16x16x32_bf16 v[20:23], v[100:103], v[214:217], v[20:23]
	v_mfma_f32_16x16x32_bf16 v[12:15], v[84:87], v[222:225], v[12:15]
	v_mfma_f32_16x16x32_bf16 v[4:7], v[100:103], v[222:225], v[4:7]
	v_mfma_f32_16x16x32_bf16 v[56:59], v[162:165], v[194:197], 0
	v_mfma_f32_16x16x32_bf16 v[48:51], v[186:189], v[194:197], 0
	v_mfma_f32_16x16x32_bf16 v[40:43], v[162:165], v[202:205], 0
	v_mfma_f32_16x16x32_bf16 v[32:35], v[186:189], v[202:205], 0
	v_mfma_f32_16x16x32_bf16 v[24:27], v[162:165], v[210:213], 0
	v_mfma_f32_16x16x32_bf16 v[16:19], v[186:189], v[210:213], 0
	v_mfma_f32_16x16x32_bf16 v[8:11], v[162:165], v[218:221], 0
	v_mfma_f32_16x16x32_bf16 v[0:3], v[186:189], v[218:221], 0
	v_mfma_f32_16x16x32_bf16 v[56:59], v[182:185], v[198:201], v[56:59]
	v_mfma_f32_16x16x32_bf16 v[48:51], v[190:193], v[198:201], v[48:51]
	v_mfma_f32_16x16x32_bf16 v[40:43], v[182:185], v[206:209], v[40:43]
	v_mfma_f32_16x16x32_bf16 v[32:35], v[190:193], v[206:209], v[32:35]
	v_mfma_f32_16x16x32_bf16 v[24:27], v[182:185], v[214:217], v[24:27]
	v_mfma_f32_16x16x32_bf16 v[16:19], v[190:193], v[214:217], v[16:19]
	v_mfma_f32_16x16x32_bf16 v[8:11], v[182:185], v[222:225], v[8:11]
	v_mfma_f32_16x16x32_bf16 v[0:3], v[190:193], v[222:225], v[0:3]
	s_barrier
	s_add_i32 s63, 0, 0x18000
	s_add_i32 s64, 0, 0x1c000
	ds_read_b128 v[80:83], v166 offset:32768
	ds_read_b128 v[84:87], v166 offset:33792
	ds_read_b128 v[96:99], v166 offset:34816
	ds_read_b128 v[100:103], v166 offset:35840
	ds_read_b128 v[162:165], v166 offset:49152
	ds_read_b128 v[182:185], v166 offset:50176
	ds_read_b128 v[186:189], v166 offset:51200
	ds_read_b128 v[190:193], v166 offset:52224
	s_add_u32 s22, s22, 0x4000
	s_addc_u32 s23, s23, 0
	s_mov_b32 m0, s47
	ds_read_b128 v[194:197], v180 offset:32768
	ds_read_b128 v[198:201], v180 offset:33792
	ds_read_b128 v[202:205], v180 offset:34816
	ds_read_b128 v[206:209], v180 offset:35840
	ds_read_b128 v[210:213], v180 offset:36864
	ds_read_b128 v[214:217], v180 offset:37888
	ds_read_b128 v[218:221], v180 offset:38912
	ds_read_b128 v[222:225], v180 offset:39936
	global_load_lds_dwordx4 v152, s[22:23]
	s_mov_b32 m0, s48
	s_nop 0
	global_load_lds_dwordx4 v148, s[22:23]
	s_waitcnt vmcnt(8)
	s_waitcnt lgkmcnt(0)
	s_barrier
; #define PG8_STAGE(bufoff, gbase, voff) do { _Pragma("unroll") for (int _i = 0; _i < 2; ++_i) \
;         __builtin_amdgcn_global_load_lds((const unsigned*)((const char*)(gbase) + (voff)[_i]), (PG8_LAS unsigned*)(lds + (bufoff) + ldsw + _i * 8192), 16, 0, 0); } while (0)
; #define PG8_LDA(dst, b, h) do { _Pragma("unroll") for (int m = 0; m < 4; ++m) _Pragma("unroll") for (int k = 0; k < 2; ++k) dst[m][k] = *(const PG8_LAS bf16x8*)(lds + PG8_SA(b, h) + aoff + m * 2048 + k * 1024); } while (0)
; #define PG8_LDB(dst, b, h) do { _Pragma("unroll") for (int n = 0; n < 2; ++n) _Pragma("unroll") for (int k = 0; k < 2; ++k) dst[n][k] = *(const PG8_LAS bf16x8*)(lds + PG8_SB(b, h) + boff + n * 2048 + k * 1024); } while (0)
; #define PG8_MMA(ai, bj, At, Bt) do { __builtin_amdgcn_s_setprio(1); _Pragma("unroll") for (int m = 0; m < 4; ++m) _Pragma("unroll") for (int n = 0; n < 2; ++n) _Pragma("unroll") for (int k = 0; k < 2; ++k) \
;         acc[ai][bj][m][n] = __builtin_amdgcn_mfma_f32_16x16x32_bf16(Bt[n][k], At[m][k], acc[ai][bj][m][n], 0, 0, 0); __builtin_amdgcn_s_setprio(0); } while (0)
; #define PG8_WAIT_V(n) asm volatile("s_waitcnt vmcnt(" #n ")" ::: "memory")
; #define PG8_WAIT_L(n) asm volatile("s_waitcnt lgkmcnt(" #n ")" ::: "memory")
; #define PG8_BAR __builtin_amdgcn_s_barrier()
; #define PG8_SCHED __builtin_amdgcn_sched_barrier(0)
; template <class Epi, class Sched, bool ALIGN_EPI>
; __device__ __forceinline__ void gemm_phase(PG8_LAS unsigned char* lds, const Gemm g, const Sched& S, const Epi& E, const int tid) {
;     ...
;             PG8_LDB(B0, 1, 0); PG8_LDB(B1, 1, 1); PG8_SCHED; PG8_LDA(At, 1, 0); PG8_STAGE(PG8_SA(0, 1), a2 + hstepA, voffA);
;             PG8_WAIT_V(8); PG8_WAIT_L(0); PG8_BAR; PG8_MMA(0, 0, At, B0); PG8_MMA(0, 1, At, B1); PG8_BAR; PG8_SCHED;
;             PG8_LDA(At, 1, 1); PG8_STAGE(PG8_SB(1, 0), b3, voffB); PG8_STAGE(PG8_SB(1, 1), b3 + hstepB, voffB); PG8_STAGE(PG8_SA(1, 0), a3, voffA);
;             PG8_WAIT_V(8); PG8_WAIT_L(0); PG8_BAR; PG8_MMA(1, 0, At, B0); PG8_MMA(1, 1, At, B1); PG8_BAR; PG8_SCHED;
;         }
	v_mfma_f32_16x16x32_bf16 v[142:145], v[80:83], v[194:197], v[142:145]
	v_mfma_f32_16x16x32_bf16 v[134:137], v[96:99], v[194:197], v[134:137]
	v_mfma_f32_16x16x32_bf16 v[124:127], v[80:83], v[202:205], v[124:127]
	v_mfma_f32_16x16x32_bf16 v[116:119], v[96:99], v[202:205], v[116:119]
	v_mfma_f32_16x16x32_bf16 v[108:111], v[80:83], v[210:213], v[108:111]
	v_mfma_f32_16x16x32_bf16 v[92:95], v[96:99], v[210:213], v[92:95]
	v_mfma_f32_16x16x32_bf16 v[76:79], v[80:83], v[218:221], v[76:79]
	v_mfma_f32_16x16x32_bf16 v[68:71], v[96:99], v[218:221], v[68:71]
	v_mfma_f32_16x16x32_bf16 v[142:145], v[84:87], v[198:201], v[142:145]
	v_mfma_f32_16x16x32_bf16 v[134:137], v[100:103], v[198:201], v[134:137]
	v_mfma_f32_16x16x32_bf16 v[124:127], v[84:87], v[206:209], v[124:127]
	v_mfma_f32_16x16x32_bf16 v[116:119], v[100:103], v[206:209], v[116:119]
	v_mfma_f32_16x16x32_bf16 v[108:111], v[84:87], v[214:217], v[108:111]
	v_mfma_f32_16x16x32_bf16 v[92:95], v[100:103], v[214:217], v[92:95]
	v_mfma_f32_16x16x32_bf16 v[76:79], v[84:87], v[222:225], v[76:79]
	v_mfma_f32_16x16x32_bf16 v[68:71], v[100:103], v[222:225], v[68:71]
	v_mfma_f32_16x16x32_bf16 v[138:141], v[162:165], v[194:197], v[138:141]
	v_mfma_f32_16x16x32_bf16 v[130:133], v[186:189], v[194:197], v[130:133]
	v_mfma_f32_16x16x32_bf16 v[120:123], v[162:165], v[202:205], v[120:123]
	v_mfma_f32_16x16x32_bf16 v[112:115], v[186:189], v[202:205], v[112:115]
	v_mfma_f32_16x16x32_bf16 v[104:107], v[162:165], v[210:213], v[104:107]
	v_mfma_f32_16x16x32_bf16 v[88:91], v[186:189], v[210:213], v[88:91]
	v_mfma_f32_16x16x32_bf16 v[72:75], v[162:165], v[218:221], v[72:75]
	v_mfma_f32_16x16x32_bf16 v[64:67], v[186:189], v[218:221], v[64:67]
	v_mfma_f32_16x16x32_bf16 v[138:141], v[182:185], v[198:201], v[138:141]
	v_mfma_f32_16x16x32_bf16 v[130:133], v[190:193], v[198:201], v[130:133]
	v_mfma_f32_16x16x32_bf16 v[120:123], v[182:185], v[206:209], v[120:123]
	v_mfma_f32_16x16x32_bf16 v[112:115], v[190:193], v[206:209], v[112:115]
	v_mfma_f32_16x16x32_bf16 v[104:107], v[182:185], v[214:217], v[104:107]
	v_mfma_f32_16x16x32_bf16 v[88:91], v[190:193], v[214:217], v[88:91]
	v_mfma_f32_16x16x32_bf16 v[72:75], v[182:185], v[222:225], v[72:75]
	v_mfma_f32_16x16x32_bf16 v[64:67], v[190:193], v[222:225], v[64:67]
	s_barrier
	s_add_u32 s22, s20, 0x8000
	s_addc_u32 s23, s21, 0
	s_add_i32 s63, s63, s42
	s_mov_b32 m0, s63
	ds_read_b128 v[194:197], v180 offset:49152
	ds_read_b128 v[198:201], v180 offset:50176
	ds_read_b128 v[202:205], v180 offset:51200
	ds_read_b128 v[206:209], v180 offset:52224
	ds_read_b128 v[210:213], v180 offset:53248
	ds_read_b128 v[214:217], v180 offset:54272
	ds_read_b128 v[218:221], v180 offset:55296
	ds_read_b128 v[222:225], v180 offset:56320
	global_load_lds_dwordx4 v150, s[22:23]
	s_add_i32 m0, s63, 0x2000
	s_add_u32 s20, s20, 0xc000
	s_addc_u32 s21, s21, 0
	global_load_lds_dwordx4 v146, s[22:23]
	s_add_i32 s22, s64, s42
	s_mov_b32 m0, s22
	s_nop 0
	global_load_lds_dwordx4 v150, s[20:21]
	s_add_i32 m0, s22, 0x2000
	s_nop 0
	global_load_lds_dwordx4 v146, s[20:21]
	s_mov_b32 m0, s51
	s_nop 0
	global_load_lds_dwordx4 v152, s[18:19]
	s_mov_b32 m0, s52
	s_nop 0
	global_load_lds_dwordx4 v148, s[18:19]
	s_waitcnt vmcnt(8)
	s_waitcnt lgkmcnt(0)
	s_barrier
	v_mfma_f32_16x16x32_bf16 v[60:63], v[80:83], v[194:197], v[60:63]
	v_mfma_f32_16x16x32_bf16 v[52:55], v[96:99], v[194:197], v[52:55]
	v_mfma_f32_16x16x32_bf16 v[44:47], v[80:83], v[202:205], v[44:47]
	v_mfma_f32_16x16x32_bf16 v[36:39], v[96:99], v[202:205], v[36:39]
	v_mfma_f32_16x16x32_bf16 v[28:31], v[80:83], v[210:213], v[28:31]
	v_mfma_f32_16x16x32_bf16 v[20:23], v[96:99], v[210:213], v[20:23]
	v_mfma_f32_16x16x32_bf16 v[12:15], v[80:83], v[218:221], v[12:15]
	v_mfma_f32_16x16x32_bf16 v[4:7], v[96:99], v[218:221], v[4:7]
	v_mfma_f32_16x16x32_bf16 v[60:63], v[84:87], v[198:201], v[60:63]
	v_mfma_f32_16x16x32_bf16 v[52:55], v[100:103], v[198:201], v[52:55]
	v_mfma_f32_16x16x32_bf16 v[44:47], v[84:87], v[206:209], v[44:47]
	v_mfma_f32_16x16x32_bf16 v[36:39], v[100:103], v[206:209], v[36:39]
	v_mfma_f32_16x16x32_bf16 v[28:31], v[84:87], v[214:217], v[28:31]
	v_mfma_f32_16x16x32_bf16 v[20:23], v[100:103], v[214:217], v[20:23]
	v_mfma_f32_16x16x32_bf16 v[12:15], v[84:87], v[222:225], v[12:15]
	v_mfma_f32_16x16x32_bf16 v[4:7], v[100:103], v[222:225], v[4:7]
	v_mfma_f32_16x16x32_bf16 v[56:59], v[162:165], v[194:197], v[56:59]
	v_mfma_f32_16x16x32_bf16 v[48:51], v[186:189], v[194:197], v[48:51]
	v_mfma_f32_16x16x32_bf16 v[40:43], v[162:165], v[202:205], v[40:43]
	v_mfma_f32_16x16x32_bf16 v[32:35], v[186:189], v[202:205], v[32:35]
	v_mfma_f32_16x16x32_bf16 v[24:27], v[162:165], v[210:213], v[24:27]
	v_mfma_f32_16x16x32_bf16 v[16:19], v[186:189], v[210:213], v[16:19]
	v_mfma_f32_16x16x32_bf16 v[8:11], v[162:165], v[218:221], v[8:11]
	v_mfma_f32_16x16x32_bf16 v[0:3], v[186:189], v[218:221], v[0:3]
	v_mfma_f32_16x16x32_bf16 v[56:59], v[182:185], v[198:201], v[56:59]
	v_mfma_f32_16x16x32_bf16 v[48:51], v[190:193], v[198:201], v[48:51]
	v_mfma_f32_16x16x32_bf16 v[40:43], v[182:185], v[206:209], v[40:43]
	v_mfma_f32_16x16x32_bf16 v[32:35], v[190:193], v[206:209], v[32:35]
	v_mfma_f32_16x16x32_bf16 v[24:27], v[182:185], v[214:217], v[24:27]
	v_mfma_f32_16x16x32_bf16 v[16:19], v[190:193], v[214:217], v[16:19]
	v_mfma_f32_16x16x32_bf16 v[8:11], v[182:185], v[222:225], v[8:11]
	v_mfma_f32_16x16x32_bf16 v[0:3], v[190:193], v[222:225], v[0:3]
	s_barrier
	s_add_i32 s62, s62, 2
	s_add_u32 s16, s16, 0x10000
	s_addc_u32 s17, s17, 0
	s_add_u32 s60, s60, 0x10000
	s_addc_u32 s61, s61, 0
; #define PG8_STAGE(bufoff, gbase, voff) do { _Pragma("unroll") for (int _i = 0; _i < 2; ++_i) \
;         __builtin_amdgcn_global_load_lds((const unsigned*)((const char*)(gbase) + (voff)[_i]), (PG8_LAS unsigned*)(lds + (bufoff) + ldsw + _i * 8192), 16, 0, 0); } while (0)
; #define PG8_LDA(dst, b, h) do { _Pragma("unroll") for (int m = 0; m < 4; ++m) _Pragma("unroll") for (int k = 0; k < 2; ++k) dst[m][k] = *(const PG8_LAS bf16x8*)(lds + PG8_SA(b, h) + aoff + m * 2048 + k * 1024); } while (0)
; #define PG8_LDB(dst, b, h) do { _Pragma("unroll") for (int n = 0; n < 2; ++n) _Pragma("unroll") for (int k = 0; k < 2; ++k) dst[n][k] = *(const PG8_LAS bf16x8*)(lds + PG8_SB(b, h) + boff + n * 2048 + k * 1024); } while (0)
; #define PG8_WAIT_V(n) asm volatile("s_waitcnt vmcnt(" #n ")" ::: "memory")
; #define PG8_WAIT_L(n) asm volatile("s_waitcnt lgkmcnt(" #n ")" ::: "memory")
; #define PG8_BAR __builtin_amdgcn_s_barrier()
; #define PG8_SCHED __builtin_amdgcn_sched_barrier(0)
; template <class Epi, class Sched, bool ALIGN_EPI>
; __device__ __forceinline__ void gemm_phase(PG8_LAS unsigned char* lds, const Gemm g, const Sched& S, const Epi& E, const int tid) {
;     ...
;         for (int t = 0; t < nt; t += 2) {
;             const bool last = (t == nt - 2);
;             const char* a1 = cA + (size_t)(t + 1) * kstepA;
;             const char* a2 = last ? nA : cA + (size_t)(t + 2) * kstepA; const char* b2 = last ? nB : cB + (size_t)(t + 2) * kstepB;
;             const char* a3 = a2 + kstepA; const char* b3 = b2 + kstepB;
;             if (last && has_next) S.a_ready(nxt);
;             PG8_LDB(B0, 0, 0); PG8_LDB(B1, 0, 1); PG8_SCHED; PG8_LDA(At, 0, 0); PG8_STAGE(PG8_SA(1, 1), a1 + hstepA, voffA);
;             PG8_WAIT_V(8); PG8_WAIT_L(0); PG8_BAR; PG8_MMA(0, 0, At, B0); PG8_MMA(0, 1, At, B1); PG8_BAR; PG8_SCHED;
;             PG8_LDA(At, 0, 1); PG8_STAGE(PG8_SB(0, 0), b2, voffB); PG8_STAGE(PG8_SB(0, 1), b2 + hstepB, voffB); PG8_STAGE(PG8_SA(0, 0), a2, voffA);
;             PG8_WAIT_V(8); PG8_WAIT_L(0); PG8_BAR; PG8_MMA(1, 0, At, B0); PG8_MMA(1, 1, At, B1); PG8_BAR; PG8_SCHED;
;             PG8_LDB(B0, 1, 0); PG8_LDB(B1, 1, 1); PG8_SCHED; PG8_LDA(At, 1, 0); PG8_STAGE(PG8_SA(0, 1), a2 + hstepA, voffA);
;             PG8_WAIT_V(8); PG8_WAIT_L(0); PG8_BAR; PG8_MMA(0, 0, At, B0); PG8_MMA(0, 1, At, B1); PG8_BAR; PG8_SCHED;
.LBB0_246:
	s_add_u32 s18, s16, 0x4000
	s_addc_u32 s19, s17, 0
	s_cmp_eq_u32 s62, 28
	s_cselect_b32 s22, s58, s18
	s_cselect_b32 s23, s11, s19
	s_cselect_b32 s20, s59, s60
	s_cselect_b32 s21, s9, s61
	s_add_u32 s18, s22, 0x8000
	s_addc_u32 s19, s23, 0
	s_add_i32 s63, 0, 0x10000
	s_add_i32 s66, 0, 0x14000
	ds_read_b128 v[80:83], v166
	ds_read_b128 v[84:87], v166 offset:1024
	ds_read_b128 v[96:99], v166 offset:2048
	ds_read_b128 v[100:103], v166 offset:3072
	ds_read_b128 v[162:165], v166 offset:16384
	ds_read_b128 v[182:185], v166 offset:17408
	ds_read_b128 v[186:189], v166 offset:18432
	ds_read_b128 v[190:193], v166 offset:19456
	s_add_i32 m0, s45, 0xc000
	ds_read_b128 v[194:197], v180
	ds_read_b128 v[198:201], v180 offset:1024
	ds_read_b128 v[202:205], v180 offset:2048
	ds_read_b128 v[206:209], v180 offset:3072
	ds_read_b128 v[210:213], v180 offset:4096
	ds_read_b128 v[214:217], v180 offset:5120
	ds_read_b128 v[218:221], v180 offset:6144
	ds_read_b128 v[222:225], v180 offset:7168
	global_load_lds_dwordx4 v158, s[16:17]
	s_add_i32 m0, s45, 0xe000
	s_nop 0
	global_load_lds_dwordx4 v160, s[16:17]
	s_waitcnt vmcnt(8)
	s_waitcnt lgkmcnt(0)
	s_barrier
	v_mfma_f32_16x16x32_bf16 v[142:145], v[80:83], v[194:197], v[142:145]
	v_mfma_f32_16x16x32_bf16 v[134:137], v[96:99], v[194:197], v[134:137]
	v_mfma_f32_16x16x32_bf16 v[124:127], v[80:83], v[202:205], v[124:127]
	v_mfma_f32_16x16x32_bf16 v[116:119], v[96:99], v[202:205], v[116:119]
	v_mfma_f32_16x16x32_bf16 v[108:111], v[80:83], v[210:213], v[108:111]
	v_mfma_f32_16x16x32_bf16 v[92:95], v[96:99], v[210:213], v[92:95]
	v_mfma_f32_16x16x32_bf16 v[76:79], v[80:83], v[218:221], v[76:79]
	v_mfma_f32_16x16x32_bf16 v[68:71], v[96:99], v[218:221], v[68:71]
	v_mfma_f32_16x16x32_bf16 v[142:145], v[84:87], v[198:201], v[142:145]
	v_mfma_f32_16x16x32_bf16 v[134:137], v[100:103], v[198:201], v[134:137]
	v_mfma_f32_16x16x32_bf16 v[124:127], v[84:87], v[206:209], v[124:127]
	v_mfma_f32_16x16x32_bf16 v[116:119], v[100:103], v[206:209], v[116:119]
	v_mfma_f32_16x16x32_bf16 v[108:111], v[84:87], v[214:217], v[108:111]
	v_mfma_f32_16x16x32_bf16 v[92:95], v[100:103], v[214:217], v[92:95]
	v_mfma_f32_16x16x32_bf16 v[76:79], v[84:87], v[222:225], v[76:79]
	v_mfma_f32_16x16x32_bf16 v[68:71], v[100:103], v[222:225], v[68:71]
	v_mfma_f32_16x16x32_bf16 v[138:141], v[162:165], v[194:197], v[138:141]
	v_mfma_f32_16x16x32_bf16 v[130:133], v[186:189], v[194:197], v[130:133]
	v_mfma_f32_16x16x32_bf16 v[120:123], v[162:165], v[202:205], v[120:123]
	v_mfma_f32_16x16x32_bf16 v[112:115], v[186:189], v[202:205], v[112:115]
	v_mfma_f32_16x16x32_bf16 v[104:107], v[162:165], v[210:213], v[104:107]
	v_mfma_f32_16x16x32_bf16 v[88:91], v[186:189], v[210:213], v[88:91]
	v_mfma_f32_16x16x32_bf16 v[72:75], v[162:165], v[218:221], v[72:75]
	v_mfma_f32_16x16x32_bf16 v[64:67], v[186:189], v[218:221], v[64:67]
	v_mfma_f32_16x16x32_bf16 v[138:141], v[182:185], v[198:201], v[138:141]
	v_mfma_f32_16x16x32_bf16 v[130:133], v[190:193], v[198:201], v[130:133]
	v_mfma_f32_16x16x32_bf16 v[120:123], v[182:185], v[206:209], v[120:123]
	v_mfma_f32_16x16x32_bf16 v[112:115], v[190:193], v[206:209], v[112:115]
	v_mfma_f32_16x16x32_bf16 v[104:107], v[182:185], v[214:217], v[104:107]
	v_mfma_f32_16x16x32_bf16 v[88:91], v[190:193], v[214:217], v[88:91]
	v_mfma_f32_16x16x32_bf16 v[72:75], v[182:185], v[222:225], v[72:75]
	v_mfma_f32_16x16x32_bf16 v[64:67], v[190:193], v[222:225], v[64:67]
	s_barrier
	s_add_i32 s63, s63, s42
	s_mov_b32 m0, s63
	ds_read_b128 v[194:197], v180 offset:16384
	ds_read_b128 v[198:201], v180 offset:17408
	ds_read_b128 v[202:205], v180 offset:18432
	ds_read_b128 v[206:209], v180 offset:19456
	ds_read_b128 v[210:213], v180 offset:20480
	ds_read_b128 v[214:217], v180 offset:21504
	ds_read_b128 v[218:221], v180 offset:22528
	ds_read_b128 v[222:225], v180 offset:23552
	global_load_lds_dwordx4 v150, s[20:21]
	s_add_i32 m0, s63, 0x2000
	s_add_u32 s64, s20, 0x4000
	s_addc_u32 s65, s21, 0
	s_add_i32 s63, s66, s42
	global_load_lds_dwordx4 v146, s[20:21]
	s_mov_b32 m0, s63
	s_nop 0
	global_load_lds_dwordx4 v150, s[64:65]
	s_add_i32 m0, s63, 0x2000
	s_nop 0
	global_load_lds_dwordx4 v146, s[64:65]
	s_mov_b32 m0, s45
	s_nop 0
	global_load_lds_dwordx4 v152, s[22:23]
	s_mov_b32 m0, s46
	s_nop 0
	global_load_lds_dwordx4 v148, s[22:23]
	s_waitcnt vmcnt(8)
	s_waitcnt lgkmcnt(0)
	s_barrier
	v_mfma_f32_16x16x32_bf16 v[60:63], v[80:83], v[194:197], v[60:63]
	v_mfma_f32_16x16x32_bf16 v[52:55], v[96:99], v[194:197], v[52:55]
	v_mfma_f32_16x16x32_bf16 v[44:47], v[80:83], v[202:205], v[44:47]
	v_mfma_f32_16x16x32_bf16 v[36:39], v[96:99], v[202:205], v[36:39]
	v_mfma_f32_16x16x32_bf16 v[28:31], v[80:83], v[210:213], v[28:31]
	v_mfma_f32_16x16x32_bf16 v[20:23], v[96:99], v[210:213], v[20:23]
	v_mfma_f32_16x16x32_bf16 v[12:15], v[80:83], v[218:221], v[12:15]
	v_mfma_f32_16x16x32_bf16 v[4:7], v[96:99], v[218:221], v[4:7]
	v_mfma_f32_16x16x32_bf16 v[60:63], v[84:87], v[198:201], v[60:63]
	v_mfma_f32_16x16x32_bf16 v[52:55], v[100:103], v[198:201], v[52:55]
	v_mfma_f32_16x16x32_bf16 v[44:47], v[84:87], v[206:209], v[44:47]
	v_mfma_f32_16x16x32_bf16 v[36:39], v[100:103], v[206:209], v[36:39]
	v_mfma_f32_16x16x32_bf16 v[28:31], v[84:87], v[214:217], v[28:31]
	v_mfma_f32_16x16x32_bf16 v[20:23], v[100:103], v[214:217], v[20:23]
	v_mfma_f32_16x16x32_bf16 v[12:15], v[84:87], v[222:225], v[12:15]
	v_mfma_f32_16x16x32_bf16 v[4:7], v[100:103], v[222:225], v[4:7]
	v_mfma_f32_16x16x32_bf16 v[56:59], v[162:165], v[194:197], v[56:59]
	v_mfma_f32_16x16x32_bf16 v[48:51], v[186:189], v[194:197], v[48:51]
	v_mfma_f32_16x16x32_bf16 v[40:43], v[162:165], v[202:205], v[40:43]
	v_mfma_f32_16x16x32_bf16 v[32:35], v[186:189], v[202:205], v[32:35]
	v_mfma_f32_16x16x32_bf16 v[24:27], v[162:165], v[210:213], v[24:27]
	v_mfma_f32_16x16x32_bf16 v[16:19], v[186:189], v[210:213], v[16:19]
	v_mfma_f32_16x16x32_bf16 v[8:11], v[162:165], v[218:221], v[8:11]
	v_mfma_f32_16x16x32_bf16 v[0:3], v[186:189], v[218:221], v[0:3]
	v_mfma_f32_16x16x32_bf16 v[56:59], v[182:185], v[198:201], v[56:59]
	v_mfma_f32_16x16x32_bf16 v[48:51], v[190:193], v[198:201], v[48:51]
	v_mfma_f32_16x16x32_bf16 v[40:43], v[182:185], v[206:209], v[40:43]
	v_mfma_f32_16x16x32_bf16 v[32:35], v[190:193], v[206:209], v[32:35]
	v_mfma_f32_16x16x32_bf16 v[24:27], v[182:185], v[214:217], v[24:27]
	v_mfma_f32_16x16x32_bf16 v[16:19], v[190:193], v[214:217], v[16:19]
	v_mfma_f32_16x16x32_bf16 v[8:11], v[182:185], v[222:225], v[8:11]
	v_mfma_f32_16x16x32_bf16 v[0:3], v[190:193], v[222:225], v[0:3]
	s_barrier
; #define PG8_STAGE(bufoff, gbase, voff) do { _Pragma("unroll") for (int _i = 0; _i < 2; ++_i) \
;         __builtin_amdgcn_global_load_lds((const unsigned*)((const char*)(gbase) + (voff)[_i]), (PG8_LAS unsigned*)(lds + (bufoff) + ldsw + _i * 8192), 16, 0, 0); } while (0)
; #define PG8_LDA(dst, b, h) do { _Pragma("unroll") for (int m = 0; m < 4; ++m) _Pragma("unroll") for (int k = 0; k < 2; ++k) dst[m][k] = *(const PG8_LAS bf16x8*)(lds + PG8_SA(b, h) + aoff + m * 2048 + k * 1024); } while (0)
; #define PG8_LDB(dst, b, h) do { _Pragma("unroll") for (int n = 0; n < 2; ++n) _Pragma("unroll") for (int k = 0; k < 2; ++k) dst[n][k] = *(const PG8_LAS bf16x8*)(lds + PG8_SB(b, h) + boff + n * 2048 + k * 1024); } while (0)
; #define PG8_MMA(ai, bj, At, Bt) do { __builtin_amdgcn_s_setprio(1); _Pragma("unroll") for (int m = 0; m < 4; ++m) _Pragma("unroll") for (int n = 0; n < 2; ++n) _Pragma("unroll") for (int k = 0; k < 2; ++k) \
;         acc[ai][bj][m][n] = __builtin_amdgcn_mfma_f32_16x16x32_bf16(Bt[n][k], At[m][k], acc[ai][bj][m][n], 0, 0, 0); __builtin_amdgcn_s_setprio(0); } while (0)
; #define PG8_WAIT_V(n) asm volatile("s_waitcnt vmcnt(" #n ")" ::: "memory")
; #define PG8_WAIT_L(n) asm volatile("s_waitcnt lgkmcnt(" #n ")" ::: "memory")
; #define PG8_BAR __builtin_amdgcn_s_barrier()
; #define PG8_SCHED __builtin_amdgcn_sched_barrier(0)
; template <class Epi, class Sched, bool ALIGN_EPI>
; __device__ __forceinline__ void gemm_phase(PG8_LAS unsigned char* lds, const Gemm g, const Sched& S, const Epi& E, const int tid) {
;     ...
;             PG8_LDB(B0, 1, 0); PG8_LDB(B1, 1, 1); PG8_SCHED; PG8_LDA(At, 1, 0); PG8_STAGE(PG8_SA(0, 1), a2 + hstepA, voffA);
;             PG8_WAIT_V(8); PG8_WAIT_L(0); PG8_BAR; PG8_MMA(0, 0, At, B0); PG8_MMA(0, 1, At, B1); PG8_BAR; PG8_SCHED;
;             PG8_LDA(At, 1, 1); PG8_STAGE(PG8_SB(1, 0), b3, voffB); PG8_STAGE(PG8_SB(1, 1), b3 + hstepB, voffB); PG8_STAGE(PG8_SA(1, 0), a3, voffA);
;             PG8_WAIT_V(8); PG8_WAIT_L(0); PG8_BAR; PG8_MMA(1, 0, At, B0); PG8_MMA(1, 1, At, B1); PG8_BAR; PG8_SCHED;
;         }
;         if constexpr (ALIGN_EPI) { if (wr == 0) PG8_BAR; }
	s_add_i32 s63, 0, 0x18000
	s_add_i32 s64, 0, 0x1c000
	ds_read_b128 v[80:83], v166 offset:32768
	ds_read_b128 v[84:87], v166 offset:33792
	ds_read_b128 v[96:99], v166 offset:34816
	ds_read_b128 v[100:103], v166 offset:35840
	ds_read_b128 v[162:165], v166 offset:49152
	ds_read_b128 v[182:185], v166 offset:50176
	ds_read_b128 v[186:189], v166 offset:51200
	ds_read_b128 v[190:193], v166 offset:52224
	s_add_u32 s22, s22, 0x4000
	s_addc_u32 s23, s23, 0
	s_mov_b32 m0, s47
	ds_read_b128 v[194:197], v180 offset:32768
	ds_read_b128 v[198:201], v180 offset:33792
	ds_read_b128 v[202:205], v180 offset:34816
	ds_read_b128 v[206:209], v180 offset:35840
	ds_read_b128 v[210:213], v180 offset:36864
	ds_read_b128 v[214:217], v180 offset:37888
	ds_read_b128 v[218:221], v180 offset:38912
	ds_read_b128 v[222:225], v180 offset:39936
	global_load_lds_dwordx4 v152, s[22:23]
	s_mov_b32 m0, s48
	s_nop 0
	global_load_lds_dwordx4 v148, s[22:23]
	s_waitcnt vmcnt(8)
	s_waitcnt lgkmcnt(0)
	s_barrier
	v_mfma_f32_16x16x32_bf16 v[142:145], v[80:83], v[194:197], v[142:145]
	v_mfma_f32_16x16x32_bf16 v[134:137], v[96:99], v[194:197], v[134:137]
	v_mfma_f32_16x16x32_bf16 v[124:127], v[80:83], v[202:205], v[124:127]
	v_mfma_f32_16x16x32_bf16 v[116:119], v[96:99], v[202:205], v[116:119]
	v_mfma_f32_16x16x32_bf16 v[108:111], v[80:83], v[210:213], v[108:111]
	v_mfma_f32_16x16x32_bf16 v[92:95], v[96:99], v[210:213], v[92:95]
	v_mfma_f32_16x16x32_bf16 v[76:79], v[80:83], v[218:221], v[76:79]
	v_mfma_f32_16x16x32_bf16 v[68:71], v[96:99], v[218:221], v[68:71]
	v_mfma_f32_16x16x32_bf16 v[142:145], v[84:87], v[198:201], v[142:145]
	v_mfma_f32_16x16x32_bf16 v[134:137], v[100:103], v[198:201], v[134:137]
	v_mfma_f32_16x16x32_bf16 v[124:127], v[84:87], v[206:209], v[124:127]
	v_mfma_f32_16x16x32_bf16 v[116:119], v[100:103], v[206:209], v[116:119]
	v_mfma_f32_16x16x32_bf16 v[108:111], v[84:87], v[214:217], v[108:111]
	v_mfma_f32_16x16x32_bf16 v[92:95], v[100:103], v[214:217], v[92:95]
	v_mfma_f32_16x16x32_bf16 v[76:79], v[84:87], v[222:225], v[76:79]
	v_mfma_f32_16x16x32_bf16 v[68:71], v[100:103], v[222:225], v[68:71]
	v_mfma_f32_16x16x32_bf16 v[138:141], v[162:165], v[194:197], v[138:141]
	v_mfma_f32_16x16x32_bf16 v[130:133], v[186:189], v[194:197], v[130:133]
	v_mfma_f32_16x16x32_bf16 v[120:123], v[162:165], v[202:205], v[120:123]
	v_mfma_f32_16x16x32_bf16 v[112:115], v[186:189], v[202:205], v[112:115]
	v_mfma_f32_16x16x32_bf16 v[104:107], v[162:165], v[210:213], v[104:107]
	v_mfma_f32_16x16x32_bf16 v[88:91], v[186:189], v[210:213], v[88:91]
	v_mfma_f32_16x16x32_bf16 v[72:75], v[162:165], v[218:221], v[72:75]
	v_mfma_f32_16x16x32_bf16 v[64:67], v[186:189], v[218:221], v[64:67]
	v_mfma_f32_16x16x32_bf16 v[138:141], v[182:185], v[198:201], v[138:141]
	v_mfma_f32_16x16x32_bf16 v[130:133], v[190:193], v[198:201], v[130:133]
	v_mfma_f32_16x16x32_bf16 v[120:123], v[182:185], v[206:209], v[120:123]
	v_mfma_f32_16x16x32_bf16 v[112:115], v[190:193], v[206:209], v[112:115]
	v_mfma_f32_16x16x32_bf16 v[104:107], v[182:185], v[214:217], v[104:107]
	v_mfma_f32_16x16x32_bf16 v[88:91], v[190:193], v[214:217], v[88:91]
	v_mfma_f32_16x16x32_bf16 v[72:75], v[182:185], v[222:225], v[72:75]
	v_mfma_f32_16x16x32_bf16 v[64:67], v[190:193], v[222:225], v[64:67]
	s_barrier
	s_add_u32 s22, s20, 0x8000
	s_addc_u32 s23, s21, 0
	s_add_i32 s63, s63, s42
	s_mov_b32 m0, s63
	ds_read_b128 v[194:197], v180 offset:49152
	ds_read_b128 v[198:201], v180 offset:50176
	ds_read_b128 v[202:205], v180 offset:51200
	ds_read_b128 v[206:209], v180 offset:52224
	ds_read_b128 v[210:213], v180 offset:53248
	ds_read_b128 v[214:217], v180 offset:54272
	ds_read_b128 v[218:221], v180 offset:55296
	ds_read_b128 v[222:225], v180 offset:56320
	global_load_lds_dwordx4 v150, s[22:23]
	s_add_i32 m0, s63, 0x2000
	s_add_u32 s20, s20, 0xc000
	s_addc_u32 s21, s21, 0
	global_load_lds_dwordx4 v146, s[22:23]
	s_add_i32 s22, s64, s42
	s_mov_b32 m0, s22
	s_nop 0
	global_load_lds_dwordx4 v150, s[20:21]
	s_add_i32 m0, s22, 0x2000
	s_nop 0
	global_load_lds_dwordx4 v146, s[20:21]
	s_mov_b32 m0, s51
	s_nop 0
	global_load_lds_dwordx4 v152, s[18:19]
	s_mov_b32 m0, s52
	s_nop 0
	global_load_lds_dwordx4 v148, s[18:19]
	s_waitcnt vmcnt(8)
	s_waitcnt lgkmcnt(0)
	s_barrier
	v_mfma_f32_16x16x32_bf16 v[60:63], v[80:83], v[194:197], v[60:63]
	v_mfma_f32_16x16x32_bf16 v[52:55], v[96:99], v[194:197], v[52:55]
	v_mfma_f32_16x16x32_bf16 v[44:47], v[80:83], v[202:205], v[44:47]
	v_mfma_f32_16x16x32_bf16 v[36:39], v[96:99], v[202:205], v[36:39]
	v_mfma_f32_16x16x32_bf16 v[28:31], v[80:83], v[210:213], v[28:31]
	v_mfma_f32_16x16x32_bf16 v[20:23], v[96:99], v[210:213], v[20:23]
	v_mfma_f32_16x16x32_bf16 v[12:15], v[80:83], v[218:221], v[12:15]
	v_mfma_f32_16x16x32_bf16 v[4:7], v[96:99], v[218:221], v[4:7]
	v_mfma_f32_16x16x32_bf16 v[60:63], v[84:87], v[198:201], v[60:63]
	v_mfma_f32_16x16x32_bf16 v[52:55], v[100:103], v[198:201], v[52:55]
	v_mfma_f32_16x16x32_bf16 v[44:47], v[84:87], v[206:209], v[44:47]
	v_mfma_f32_16x16x32_bf16 v[36:39], v[100:103], v[206:209], v[36:39]
	v_mfma_f32_16x16x32_bf16 v[28:31], v[84:87], v[214:217], v[28:31]
	v_mfma_f32_16x16x32_bf16 v[20:23], v[100:103], v[214:217], v[20:23]
	v_mfma_f32_16x16x32_bf16 v[12:15], v[84:87], v[222:225], v[12:15]
	v_mfma_f32_16x16x32_bf16 v[4:7], v[100:103], v[222:225], v[4:7]
	v_mfma_f32_16x16x32_bf16 v[56:59], v[162:165], v[194:197], v[56:59]
	v_mfma_f32_16x16x32_bf16 v[48:51], v[186:189], v[194:197], v[48:51]
	v_mfma_f32_16x16x32_bf16 v[40:43], v[162:165], v[202:205], v[40:43]
	v_mfma_f32_16x16x32_bf16 v[32:35], v[186:189], v[202:205], v[32:35]
	v_mfma_f32_16x16x32_bf16 v[24:27], v[162:165], v[210:213], v[24:27]
	v_mfma_f32_16x16x32_bf16 v[16:19], v[186:189], v[210:213], v[16:19]
	v_mfma_f32_16x16x32_bf16 v[8:11], v[162:165], v[218:221], v[8:11]
	v_mfma_f32_16x16x32_bf16 v[0:3], v[186:189], v[218:221], v[0:3]
	v_mfma_f32_16x16x32_bf16 v[56:59], v[182:185], v[198:201], v[56:59]
	v_mfma_f32_16x16x32_bf16 v[48:51], v[190:193], v[198:201], v[48:51]
	v_mfma_f32_16x16x32_bf16 v[40:43], v[182:185], v[206:209], v[40:43]
	v_mfma_f32_16x16x32_bf16 v[32:35], v[190:193], v[206:209], v[32:35]
	v_mfma_f32_16x16x32_bf16 v[24:27], v[182:185], v[214:217], v[24:27]
	v_mfma_f32_16x16x32_bf16 v[16:19], v[190:193], v[214:217], v[16:19]
	v_mfma_f32_16x16x32_bf16 v[8:11], v[182:185], v[222:225], v[8:11]
	v_mfma_f32_16x16x32_bf16 v[0:3], v[190:193], v[222:225], v[0:3]
	s_barrier
	s_add_i32 s62, s62, 2
	s_add_u32 s16, s16, 0x10000
	s_addc_u32 s17, s17, 0
	s_add_u32 s60, s60, 0x10000
	s_addc_u32 s61, s61, 0
	s_cmp_gt_u32 s62, 29
	s_cbranch_scc0 .LBB0_246
	s_and_b64 vcc, exec, s[6:7]
	s_cbranch_vccz .LBB0_249
